# P4->P5 grid barrier removed (P5 tiles consume only what the same workgroup produced in P4; workgroup barrier + L1 invalidate kept), on top of P5 SGPR prefetch
# baseline (speedup 1.0000x reference)
; __device__ __forceinline__ unsigned xb_ld(unsigned* p)              { return __hip_atomic_load(p, __ATOMIC_RELAXED, __HIP_MEMORY_SCOPE_AGENT); }
; __device__ __forceinline__ unsigned xb_add(unsigned* p, unsigned v) { return __hip_atomic_fetch_add(p, v, __ATOMIC_RELAXED, __HIP_MEMORY_SCOPE_AGENT); }
; #define XB_SPIN(cond, bar) do { unsigned _sp = 0; while (cond) { __builtin_amdgcn_s_sleep(1); \
;     if ((++_sp & 255u) == 0u) { if (xb_ld(&(bar)[XB_TMO])) break; if (_sp > XB_SPIN_CAP) { atomicAdd(&(bar)[XB_TMO], 1u); break; } } } } while (0)
; __device__ __forceinline__ void xcd_barrier(const XcdBarrier& b) {
;     asm volatile("s_waitcnt vmcnt(0)" ::: "memory");
;     __syncthreads();
;     if (threadIdx.x == 0) {
;         unsigned* bar = b.bar;
;         __builtin_amdgcn_s_waitcnt(0);
;         unsigned nloc = b.st[0], nx = b.st[1];
;         if (nloc == 0u) { xcd_barrier_complete(bar, b.x, nloc, nx); b.st[0] = nloc; b.st[1] = nx; }
;         const unsigned old = xb_add(&bar[XB_XSUB(b.x)], 1u);
;         const unsigned gen = old / nloc;
;         if (old + 1u == (gen + 1u) * nloc) {
;             __builtin_amdgcn_fence(__ATOMIC_RELEASE, "agent");
;             asm volatile("s_waitcnt vmcnt(0)" ::: "memory");
;             const unsigned og = xb_add(&bar[XB_TOP], 1u);
;             const unsigned tg = og / nx;
;             if (og + 1u == (tg + 1u) * nx) xb_add(&bar[XB_TOPGEN], 1u);
;             else XB_SPIN(xb_ld(&bar[XB_TOPGEN]) == tg, bar);
;             __builtin_amdgcn_fence(__ATOMIC_ACQUIRE, "agent");
;             xb_add(&bar[XB_XGEN(b.x)], 1u);
;             asm volatile("s_waitcnt vmcnt(0)" ::: "memory");
;         } else {
;             XB_SPIN(xb_ld(&bar[XB_XGEN(b.x)]) == gen, bar);
;             __builtin_amdgcn_fence(__ATOMIC_ACQUIRE, "agent");
;             asm volatile("s_waitcnt vmcnt(0)" ::: "memory");
;         }
;     }
;     __syncthreads();
.LBB0_602:
	v_readlane_b32 s24, v254, 15
	v_readlane_b32 s82, v254, 13
	v_mov_b32_e32 v1, v0
	s_and_b64 vcc, exec, s[2:3]
	v_readlane_b32 s25, v254, 16
	v_readlane_b32 s83, v254, 14
	s_cbranch_vccnz .LBB0_653
	v_mov_b32_e32 v1, v0
	s_cmp_lt_u32 s83, 6
	s_cbranch_scc1 .LBB0_653
	s_waitcnt vmcnt(0)
	v_cmp_eq_u32_e32 vcc, 0, v0
	s_barrier
	s_mov_b64 s[2:3], exec
	buffer_inv sc1
	s_waitcnt vmcnt(0)
	s_branch .LBB0_652
	s_add_i32 s0, 0, 0x22000
	v_mov_b32_e32 v1, s0
	s_waitcnt vmcnt(0) expcnt(0) lgkmcnt(0)
	ds_read_b32 v3, v1
	s_add_i32 s0, 0, 0x22004
	v_mov_b32_e32 v1, s0
	ds_read_b32 v1, v1
	s_waitcnt lgkmcnt(1)
	v_cmp_ne_u32_e32 vcc, 0, v3
	s_cbranch_vccnz .LBB0_620
	v_readlane_b32 s0, v254, 5
	v_readlane_b32 s1, v254, 6
	s_load_dwordx2 s[6:7], s[0:1], 0x4
	s_add_u32 s0, s62, 0x1000
	s_addc_u32 s1, s63, 0
	s_add_u32 s4, s62, 0x1100
	s_addc_u32 s5, s63, 0
	v_readlane_b32 s8, v254, 2
	s_waitcnt lgkmcnt(0)
	s_mul_i32 s16, s6, s8
	s_add_u32 s6, s62, 0x1200
	s_mul_i32 s16, s16, s7
	s_addc_u32 s7, s63, 0
	v_readlane_b32 s9, v254, 3
	s_add_u32 s8, s62, 0x1300
	s_addc_u32 s9, s63, 0
	s_mov_b32 s17, 1
	v_mov_b32_e32 v17, 0
	s_branch .LBB0_608
